# v010 + GEMM phase prologue: K-tile 1's six LDS-DMA pieces issued before the first wait/barrier (one cold round trip instead of two at every GEMM phase start)
# baseline (speedup 1.0000x reference)
;     __device__ __forceinline__ size_t boff(const Unit& u) const { return (size_t)__builtin_amdgcn_readfirstlane(panel_e[u.pm]) * estride; }
; #define PG8_SETA(v, u) do { if constexpr (Sched::GATHER) { _Pragma("unroll") for (int h_ = 0; h_ < 2; ++h_) _Pragma("unroll") for (int i_ = 0; i_ < 2; ++i_) { \
;         int R_, C_; stage_rc(tid * 16 + i_ * 8192, R_, C_); int tok_ = S.arow[(u).pm * BM + h_ * HALF + R_]; tok_ = tok_ < 0 ? 0 : tok_; (v)[h_][i_] = (unsigned)(tok_ * K + C_) * 2u; } } } while (0)
; #define PG8_STAGE_A(bufoff, h, ptr, nsel) do { if constexpr (Sched::GATHER) { if (nsel) PG8_STAGE_X(bufoff, ptr, vAn[h], PG8_A_AUX); else PG8_STAGE_X(bufoff, ptr, vAc[h], PG8_A_AUX); } \
;         else PG8_STAGE_X(bufoff, (ptr) + (h) * hstep, voffA, PG8_A_AUX); } while (0)
; #define PG8_STAGE(bufoff, gbase, voff) PG8_STAGE_X(bufoff, gbase, voff, PG8_B_AUX)
; #define PG8_WAIT_V(n) asm volatile("s_waitcnt vmcnt(" #n ")" ::: "memory")
; #define PG8_BAR __builtin_amdgcn_s_barrier()
; template <class Epi, class Sched, bool ALIGN_EPI = false, bool SP2 = false>
; __device__ __forceinline__ void gemm_phase(PG8_LAS unsigned char* lds, const Gemm g, const Sched& S, const Epi& E) {
;     ...
;     const char* cA = Sched::GATHER ? (const char*)g.A : (const char*)g.A + (size_t)cur.pm * tstep; PG8_SETA(vAc, cur); const char* cB = (const char*)g.Bt + S.boff(cur) + (size_t)cur.pn * tstep;
;     S.a_ready(cur);
;     if constexpr (SP2) {
;         PG8_STAGE(PG8_SB(0, 0), cB, voffB); PG8_STAGE(PG8_SB(0, 1), cB + hstep, voffB); PG8_STAGE_A(PG8_SA(0, 0), 0, cA, false); PG8_STAGE_A(PG8_SA(0, 1), 1, cA, false);
;         if (wr == 1) PG8_BAR;
;         PG8_WAIT_V(2); PG8_BAR;
;         PG8_STAGE(PG8_SB(1, 0), cB + kstep, voffB); PG8_STAGE_A(PG8_SA(1, 0), 0, cA + kstep, false); PG8_STAGE(PG8_SB(1, 1), cB + hstep + kstep, voffB);
;         PG8_WAIT_V(6); PG8_BAR;
.LBB13_231:
	s_add_i32 s41, s3, 0x18000
	s_add_i32 s45, s41, s40
	s_and_b32 s7, s6, 3
	v_lshl_add_u64 v[4:5], v[4:5], 0, s[54:55]
	s_mov_b32 m0, s45
	s_add_i32 s46, s45, 0x2000
	s_add_i32 s47, s3, s40
	s_add_i32 s42, s3, 0x1c000
	s_ashr_i32 s43, s29, 31
	s_lshl_b32 s44, s4, 6
	s_lshl_b32 s9, s4, 13
	s_lshl_b32 s11, s7, 12
	global_load_lds_dwordx4 v[4:5], off
	v_lshl_add_u64 v[4:5], v[6:7], 0, s[54:55]
	s_mov_b32 m0, s46
	s_add_i32 s50, s47, 0x8000
	s_add_i32 s51, s47, 0xa000
	global_load_lds_dwordx4 v[4:5], off
	v_lshl_add_u64 v[4:5], v[8:9], 0, s[54:55]
	s_mov_b32 m0, s50
	s_add_u32 s4, s24, 0x40080
	global_load_lds_dwordx4 v[4:5], off
	v_lshl_add_u64 v[4:5], v[10:11], 0, s[54:55]
	s_mov_b32 m0, s51
	s_addc_u32 s5, s25, 0
	s_add_i32 s56, s42, s40
	global_load_lds_dwordx4 v[4:5], off
	v_lshl_add_u64 v[4:5], s[4:5], 0, v[142:143]
	s_mov_b32 m0, s56
	s_add_i32 s57, s56, 0x2000
	global_load_lds_dwordx4 v[4:5], off
	v_lshl_add_u64 v[4:5], s[4:5], 0, v[146:147]
	s_mov_b32 m0, s57
	s_cmpk_lt_u32 s2, 0x100
	global_load_lds_dwordx4 v[4:5], off
	s_waitcnt vmcnt(8)
	s_barrier
	s_mov_b64 s[4:5], 0x22800000
	s_cselect_b64 s[14:15], -1, 0
	s_cmp_lt_u32 s7, 2
	v_lshl_add_u64 v[148:149], v[2:3], 0, s[4:5]
	v_bfe_u32 v4, v12, 4, 2
	s_cselect_b64 s[4:5], -1, 0
	s_lshl_b32 s2, s6, 7
	v_lshlrev_b32_e32 v5, 3, v4
	s_and_b32 s76, s2, 0x80
	v_lshlrev_b32_e32 v6, 4, v4
	v_lshl_or_b32 v168, s7, 5, v5
	v_lshl_add_u64 v[2:3], v[2:3], 0, s[76:77]
	v_lshlrev_b32_e32 v4, 5, v4
	v_mov_b32_e32 v5, v98
	v_lshl_add_u64 v[2:3], v[2:3], 0, v[4:5]
	s_mov_b64 s[6:7], 0x250000
	v_lshl_add_u64 v[150:151], v[2:3], 0, s[6:7]
	v_lshlrev_b32_e32 v2, 14, v13
	v_and_b32_e32 v2, 0xffff8000, v2
	v_lshl_add_u32 v2, v14, 11, v2
	v_and_b32_e32 v3, 1, v13
	v_lshl_or_b32 v2, v3, 6, v2
	v_lshl_add_u32 v152, v15, 1, v2
	v_lshlrev_b32_e32 v2, 14, v16
	v_and_b32_e32 v1, 15, v12
	v_lshlrev_b32_e32 v7, 2, v12
	v_and_b32_e32 v2, 0xffff8000, v2
	v_lshl_or_b32 v6, v1, 6, v6
	v_and_b32_e32 v7, 32, v7
	s_waitcnt vmcnt(6)
	v_lshl_add_u32 v2, v17, 11, v2
	v_and_b32_e32 v3, 1, v16
	v_bitop3_b32 v8, v6, s9, v7 bitop3:0xde
	v_lshl_or_b32 v2, v3, 6, v2
	v_bitop3_b32 v99, v6, s11, v7 bitop3:0xde
	v_or_b32_e32 v169, 16, v1
	v_or_b32_e32 v170, 32, v1
	v_or_b32_e32 v171, 48, v1
	v_mov_b32_e32 v153, v98
	v_lshl_add_u32 v154, v18, 1, v2
	v_mov_b32_e32 v155, v98
	s_mov_b32 s58, 0
	v_add_u32_e32 v172, s3, v8
	s_barrier
	s_branch .LBB13_234

; #define PG8_STAGE_A(bufoff, h, ptr, nsel) do { if constexpr (Sched::GATHER) { if (nsel) PG8_STAGE_X(bufoff, ptr, vAn[h], PG8_A_AUX); else PG8_STAGE_X(bufoff, ptr, vAc[h], PG8_A_AUX); } \
;         else PG8_STAGE_X(bufoff, (ptr) + (h) * hstep, voffA, PG8_A_AUX); } while (0)
; #define PG8_STAGE(bufoff, gbase, voff) PG8_STAGE_X(bufoff, gbase, voff, PG8_B_AUX)
; #define PG8_WAIT_V(n) asm volatile("s_waitcnt vmcnt(" #n ")" ::: "memory")
; #define PG8_BAR __builtin_amdgcn_s_barrier()
; template <class Epi, class Sched, bool ALIGN_EPI = false, bool SP2 = false>
; __device__ __forceinline__ void gemm_phase(PG8_LAS unsigned char* lds, const Gemm g, const Sched& S, const Epi& E) {
;     ...
;         PG8_STAGE(PG8_SB(0, 0), cB, voffB); PG8_STAGE(PG8_SB(0, 1), cB + hstep, voffB); PG8_STAGE_A(PG8_SA(0, 0), 0, cA, false); PG8_STAGE_A(PG8_SA(0, 1), 1, cA, false);
;         if (wr == 1) PG8_BAR;
;         PG8_WAIT_V(2); PG8_BAR;
;         PG8_STAGE(PG8_SB(1, 0), cB + kstep, voffB); PG8_STAGE_A(PG8_SA(1, 0), 0, cA + kstep, false); PG8_STAGE(PG8_SB(1, 1), cB + hstep + kstep, voffB);
;         PG8_WAIT_V(6); PG8_BAR;
.LBB13_812:
	v_lshrrev_b32_e32 v18, 1, v16
	v_and_b32_e32 v18, 24, v18
	v_and_b32_e32 v17, 15, v16
	v_lshlrev_b32_e32 v19, 1, v18
	v_lshlrev_b32_e32 v16, 2, v16
	s_sext_i32_i8 s23, s4
	v_lshl_or_b32 v99, s14, 6, v17
	v_lshl_or_b32 v17, v17, 6, v19
	s_lshl_b32 s4, s14, 13
	v_and_b32_e32 v16, 32, v16
	v_bitop3_b32 v19, v17, s4, v16 bitop3:0xde
	s_lshl_b32 s4, s13, 5
	s_add_i32 s69, s50, s12
	s_and_b32 s4, s4, 0x60
	v_lshl_add_u64 v[8:9], v[8:9], 0, s[54:55]
	s_mov_b32 m0, s69
	s_add_i32 s88, s69, 0x2000
	s_lshl_b32 s13, s4, 7
	global_load_lds_dwordx4 v[8:9], off
	v_lshl_add_u64 v[6:7], v[6:7], 0, s[54:55]
	s_mov_b32 m0, s88
	s_add_i32 s89, s58, 0x8000
	s_add_i32 s94, s58, 0xa000
	global_load_lds_dwordx4 v[6:7], off
	v_lshl_add_u64 v[2:3], v[2:3], 0, s[54:55]
	s_mov_b32 m0, s89
	s_add_u32 s14, s26, 0x40080
	global_load_lds_dwordx4 v[2:3], off
	v_lshl_add_u64 v[2:3], v[4:5], 0, s[54:55]
	s_mov_b32 m0, s94
	s_addc_u32 s15, s27, 0
	s_add_i32 s38, s51, s12
	global_load_lds_dwordx4 v[2:3], off
	v_lshl_add_u64 v[2:3], s[14:15], 0, v[140:141]
	s_mov_b32 m0, s38
	s_add_i32 s95, s38, 0x2000
	global_load_lds_dwordx4 v[2:3], off
	v_lshl_add_u64 v[2:3], s[14:15], 0, v[136:137]
	s_mov_b32 m0, s95
	s_cmpk_lt_u32 s5, 0x100
	global_load_lds_dwordx4 v[2:3], off
	s_waitcnt vmcnt(8)
	s_barrier
	v_lshlrev_b32_e32 v2, 14, v14
	v_and_b32_e32 v2, 0xffff8000, v2
	v_lshl_add_u32 v2, v13, 11, v2
	v_and_b32_e32 v3, 1, v14
	v_lshl_or_b32 v2, v3, 6, v2
	v_lshl_add_u32 v144, v15, 1, v2
	v_lshlrev_b32_e32 v2, 14, v10
	v_and_b32_e32 v2, 0xffff8000, v2
	s_waitcnt vmcnt(6)
	v_lshl_add_u32 v2, v11, 11, v2
	v_and_b32_e32 v3, 1, v10
	v_lshl_or_b32 v2, v3, 6, v2
	v_bitop3_b32 v152, v17, s13, v16 bitop3:0xde
	s_cselect_b64 s[14:15], -1, 0
	v_or_b32_e32 v153, s4, v18
	v_mov_b32_e32 v145, v98
	v_lshl_add_u32 v146, v12, 1, v2
	v_mov_b32_e32 v147, v98
	s_mov_b32 s34, 0
	v_add_u32_e32 v154, s36, v19
	s_barrier
	s_branch .LBB13_815

; #define PG8_STAGE_A(bufoff, h, ptr, nsel) do { if constexpr (Sched::GATHER) { if (nsel) PG8_STAGE_X(bufoff, ptr, vAn[h], PG8_A_AUX); else PG8_STAGE_X(bufoff, ptr, vAc[h], PG8_A_AUX); } \
;         else PG8_STAGE_X(bufoff, (ptr) + (h) * hstep, voffA, PG8_A_AUX); } while (0)
; #define PG8_STAGE(bufoff, gbase, voff) PG8_STAGE_X(bufoff, gbase, voff, PG8_B_AUX)
; #define PG8_WAIT_V(n) asm volatile("s_waitcnt vmcnt(" #n ")" ::: "memory")
; #define PG8_BAR __builtin_amdgcn_s_barrier()
; template <class Epi, class Sched, bool ALIGN_EPI = false, bool SP2 = false>
; __device__ __forceinline__ void gemm_phase(PG8_LAS unsigned char* lds, const Gemm g, const Sched& S, const Epi& E) {
;     ...
;         PG8_STAGE(PG8_SB(0, 0), cB, voffB); PG8_STAGE(PG8_SB(0, 1), cB + hstep, voffB); PG8_STAGE_A(PG8_SA(0, 0), 0, cA, false); PG8_STAGE_A(PG8_SA(0, 1), 1, cA, false);
;         if (wr == 1) PG8_BAR;
;         PG8_WAIT_V(2); PG8_BAR;
;         PG8_STAGE(PG8_SB(1, 0), cB + kstep, voffB); PG8_STAGE_A(PG8_SA(1, 0), 0, cA + kstep, false); PG8_STAGE(PG8_SB(1, 1), cB + hstep + kstep, voffB);
;         PG8_WAIT_V(6); PG8_BAR;
.LBB13_834:
	v_lshrrev_b32_e32 v18, 1, v16
	v_and_b32_e32 v18, 24, v18
	v_and_b32_e32 v17, 15, v16
	v_lshlrev_b32_e32 v19, 1, v18
	v_lshlrev_b32_e32 v16, 2, v16
	s_sext_i32_i8 s13, s4
	v_lshl_or_b32 v99, s14, 6, v17
	v_lshl_or_b32 v17, v17, 6, v19
	s_lshl_b32 s4, s14, 13
	v_and_b32_e32 v16, 32, v16
	v_bitop3_b32 v19, v17, s4, v16 bitop3:0xde
	s_lshl_b32 s4, s11, 5
	s_add_i32 s57, s50, s10
	s_and_b32 s4, s4, 0x60
	v_lshl_add_u64 v[8:9], v[8:9], 0, s[54:55]
	s_mov_b32 m0, s57
	s_add_i32 s58, s57, 0x2000
	s_lshl_b32 s11, s4, 7
	global_load_lds_dwordx4 v[8:9], off
	v_lshl_add_u64 v[6:7], v[6:7], 0, s[54:55]
	s_mov_b32 m0, s58
	s_add_i32 s59, s48, 0x8000
	s_add_i32 s61, s48, 0xa000
	global_load_lds_dwordx4 v[6:7], off
	v_lshl_add_u64 v[2:3], v[2:3], 0, s[54:55]
	s_mov_b32 m0, s59
	s_add_u32 s14, s24, 0x40080
	global_load_lds_dwordx4 v[2:3], off
	v_lshl_add_u64 v[2:3], v[4:5], 0, s[54:55]
	s_mov_b32 m0, s61
	s_addc_u32 s15, s25, 0
	s_add_i32 s68, s51, s10
	global_load_lds_dwordx4 v[2:3], off
	v_lshl_add_u64 v[2:3], s[14:15], 0, v[140:141]
	s_mov_b32 m0, s68
	s_add_i32 s69, s68, 0x2000
	global_load_lds_dwordx4 v[2:3], off
	v_lshl_add_u64 v[2:3], s[14:15], 0, v[136:137]
	s_mov_b32 m0, s69
	s_cmpk_lt_u32 s5, 0x100
	global_load_lds_dwordx4 v[2:3], off
	s_waitcnt vmcnt(8)
	s_barrier
	v_lshlrev_b32_e32 v2, 14, v14
	v_and_b32_e32 v2, 0xffff8000, v2
	v_lshl_add_u32 v2, v13, 11, v2
	v_and_b32_e32 v3, 1, v14
	v_lshl_or_b32 v2, v3, 6, v2
	v_lshl_add_u32 v144, v15, 1, v2
	v_lshlrev_b32_e32 v2, 14, v10
	v_and_b32_e32 v2, 0xffff8000, v2
	s_waitcnt vmcnt(6)
	v_lshl_add_u32 v2, v11, 11, v2
	v_and_b32_e32 v3, 1, v10
	v_lshl_or_b32 v2, v3, 6, v2
	v_bitop3_b32 v152, v17, s11, v16 bitop3:0xde
	s_cselect_b64 s[10:11], -1, 0
	v_or_b32_e32 v153, s4, v18
	v_mov_b32_e32 v145, v98
	v_lshl_add_u32 v146, v12, 1, v2
	v_mov_b32_e32 v147, v98
	s_mov_b32 s88, 0
	v_add_u32_e32 v154, s36, v19
	s_barrier
	s_branch .LBB13_837

; #define PG8_STAGE_A(bufoff, h, ptr, nsel) do { if constexpr (Sched::GATHER) { if (nsel) PG8_STAGE_X(bufoff, ptr, vAn[h], PG8_A_AUX); else PG8_STAGE_X(bufoff, ptr, vAc[h], PG8_A_AUX); } \
;         else PG8_STAGE_X(bufoff, (ptr) + (h) * hstep, voffA, PG8_A_AUX); } while (0)
; #define PG8_STAGE(bufoff, gbase, voff) PG8_STAGE_X(bufoff, gbase, voff, PG8_B_AUX)
; #define PG8_WAIT_V(n) asm volatile("s_waitcnt vmcnt(" #n ")" ::: "memory")
; #define PG8_BAR __builtin_amdgcn_s_barrier()
; template <class Epi, class Sched, bool ALIGN_EPI = false, bool SP2 = false>
; __device__ __forceinline__ void gemm_phase(PG8_LAS unsigned char* lds, const Gemm g, const Sched& S, const Epi& E) {
;     ...
;         PG8_STAGE(PG8_SB(0, 0), cB, voffB); PG8_STAGE(PG8_SB(0, 1), cB + hstep, voffB); PG8_STAGE_A(PG8_SA(0, 0), 0, cA, false); PG8_STAGE_A(PG8_SA(0, 1), 1, cA, false);
;         if (wr == 1) PG8_BAR;
;         PG8_WAIT_V(2); PG8_BAR;
;         PG8_STAGE(PG8_SB(1, 0), cB + kstep, voffB); PG8_STAGE_A(PG8_SA(1, 0), 0, cA + kstep, false); PG8_STAGE(PG8_SB(1, 1), cB + hstep + kstep, voffB);
;         PG8_WAIT_V(6); PG8_BAR;
.LBB13_916:
	s_lshl_b64 s[14:15], s[10:11], 2
	v_readlane_b32 s20, v249, 39
	v_readlane_b32 s21, v249, 40
	s_add_u32 s7, s20, s14
	s_addc_u32 s14, s21, s15
	s_and_b64 s[4:5], s[4:5], exec
	s_cselect_b32 s15, s14, 0
	s_cselect_b32 s14, s7, 0
	s_lshl_b32 s4, s17, 5
	s_add_i32 s53, s40, 0x18000
	s_and_b32 s20, s4, 0x60
	s_add_i32 s56, s53, s19
	s_lshl_b32 s7, s18, 13
	s_lshl_b32 s17, s20, 7
	v_lshl_add_u64 v[8:9], v[8:9], 0, s[54:55]
	s_mov_b32 m0, s56
	s_add_i32 s57, s56, 0x2000
	s_add_i32 s58, s49, 0x8000
	s_add_i32 s59, s49, 0xa000
	global_load_lds_dwordx4 v[8:9], off
	v_lshl_add_u64 v[6:7], v[6:7], 0, s[54:55]
	s_mov_b32 m0, s57
	s_add_u32 s4, s34, 0x40080
	global_load_lds_dwordx4 v[6:7], off
	v_lshl_add_u64 v[2:3], v[2:3], 0, s[54:55]
	s_mov_b32 m0, s58
	s_addc_u32 s5, s35, 0
	s_add_i32 s60, s40, 0x1c000
	global_load_lds_dwordx4 v[2:3], off
	v_lshl_add_u64 v[2:3], v[4:5], 0, s[54:55]
	s_mov_b32 m0, s59
	s_add_i32 s61, s60, s19
	global_load_lds_dwordx4 v[2:3], off
	v_lshl_add_u64 v[2:3], s[4:5], 0, v[162:163]
	s_mov_b32 m0, s61
	s_add_i32 s64, s61, 0x2000
	global_load_lds_dwordx4 v[2:3], off
	v_lshl_add_u64 v[2:3], s[4:5], 0, v[166:167]
	s_mov_b32 m0, s64
	s_cmpk_lt_u32 s16, 0x100
	global_load_lds_dwordx4 v[2:3], off
	s_waitcnt vmcnt(8)
	s_barrier
	v_lshrrev_b32_e32 v3, 1, v10
	v_and_b32_e32 v3, 24, v3
	v_and_b32_e32 v2, 15, v10
	v_lshlrev_b32_e32 v4, 1, v3
	v_lshl_or_b32 v99, s18, 6, v2
	v_lshl_or_b32 v2, v2, 6, v4
	v_lshlrev_b32_e32 v4, 2, v10
	v_and_b32_e32 v4, 32, v4
	v_bitop3_b32 v5, v2, s7, v4 bitop3:0xde
	v_bitop3_b32 v184, v2, s17, v4 bitop3:0xde
	v_lshlrev_b32_e32 v2, 14, v11
	v_and_b32_e32 v2, 0xffff8000, v2
	v_or_b32_e32 v185, s20, v3
	v_lshl_add_u32 v2, v12, 11, v2
	v_and_b32_e32 v3, 1, v11
	v_lshl_or_b32 v2, v3, 6, v2
	v_lshl_add_u32 v170, v13, 1, v2
	v_lshlrev_b32_e32 v2, 14, v14
	v_and_b32_e32 v2, 0xffff8000, v2
	s_waitcnt vmcnt(6)
	s_cselect_b64 s[16:17], -1, 0
	s_ashr_i32 s69, s0, 31
	s_ashr_i32 s72, s3, 31
	v_lshl_add_u32 v2, v15, 11, v2
	v_and_b32_e32 v3, 1, v14
	s_mov_b64 s[4:5], 0x202000
	s_cmp_lg_u64 s[14:15], 0
	v_lshl_or_b32 v2, v3, 6, v2
	v_lshl_add_u64 v[168:169], v[158:159], 0, s[4:5]
	s_mov_b32 s68, 0
	s_cselect_b64 s[18:19], -1, 0
	v_mov_b32_e32 v171, v98
	v_lshl_add_u32 v172, v16, 1, v2
	v_mov_b32_e32 v173, v98
	v_add_u32_e32 v186, s40, v5
	s_barrier
	s_branch .LBB13_919

; #define PG8_STAGE_A(bufoff, h, ptr, nsel) do { if constexpr (Sched::GATHER) { if (nsel) PG8_STAGE_X(bufoff, ptr, vAn[h], PG8_A_AUX); else PG8_STAGE_X(bufoff, ptr, vAc[h], PG8_A_AUX); } \
;         else PG8_STAGE_X(bufoff, (ptr) + (h) * hstep, voffA, PG8_A_AUX); } while (0)
; #define PG8_STAGE(bufoff, gbase, voff) PG8_STAGE_X(bufoff, gbase, voff, PG8_B_AUX)
; #define PG8_WAIT_V(n) asm volatile("s_waitcnt vmcnt(" #n ")" ::: "memory")
; #define PG8_BAR __builtin_amdgcn_s_barrier()
; template <class Epi, class Sched, bool ALIGN_EPI = false, bool SP2 = false>
; __device__ __forceinline__ void gemm_phase(PG8_LAS unsigned char* lds, const Gemm g, const Sched& S, const Epi& E) {
;     ...
;         PG8_STAGE(PG8_SB(0, 0), cB, voffB); PG8_STAGE(PG8_SB(0, 1), cB + hstep, voffB); PG8_STAGE_A(PG8_SA(0, 0), 0, cA, false); PG8_STAGE_A(PG8_SA(0, 1), 1, cA, false);
;         if (wr == 1) PG8_BAR;
;         PG8_WAIT_V(2); PG8_BAR;
;         PG8_STAGE(PG8_SB(1, 0), cB + kstep, voffB); PG8_STAGE_A(PG8_SA(1, 0), 0, cA + kstep, false); PG8_STAGE(PG8_SB(1, 1), cB + hstep + kstep, voffB);
;         PG8_WAIT_V(6); PG8_BAR;
.LBB13_1402:
	v_lshrrev_b32_e32 v18, 1, v8
	v_and_b32_e32 v18, 24, v18
	s_lshl_b32 s12, s12, 5
	v_mov_b32_e32 v137, v98
	v_and_b32_e32 v9, 15, v8
	v_lshlrev_b32_e32 v19, 1, v18
	v_lshlrev_b32_e32 v8, 2, v8
	s_and_b32 s18, s12, 0x60
	v_lshl_add_u64 v[10:11], s[34:35], 0, v[136:137]
	v_mov_b32_e32 v133, v98
	v_lshl_or_b32 v1, s13, 6, v9
	v_lshl_or_b32 v9, v9, 6, v19
	s_lshl_b32 s13, s13, 13
	v_and_b32_e32 v8, 32, v8
	s_lshl_b32 s12, s18, 7
	s_add_i32 s64, s51, s7
	v_lshl_add_u64 v[12:13], s[34:35], 0, v[132:133]
	v_mov_b32_e32 v139, v98
	v_bitop3_b32 v19, v9, s13, v8 bitop3:0xde
	v_bitop3_b32 v99, v9, s12, v8 bitop3:0xde
	v_lshl_add_u64 v[8:9], v[10:11], 0, s[54:55]
	s_mov_b32 m0, s64
	s_add_i32 s68, s64, 0x2000
	v_lshl_add_u64 v[14:15], s[30:31], 0, v[138:139]
	v_mov_b32_e32 v135, v98
	global_load_lds_dwordx4 v[8:9], off
	v_lshl_add_u64 v[8:9], v[12:13], 0, s[54:55]
	s_mov_b32 m0, s68
	s_add_i32 s69, s58, 0x8000
	s_add_i32 s72, s58, 0xa000
	v_lshl_add_u64 v[16:17], s[30:31], 0, v[134:135]
	global_load_lds_dwordx4 v[8:9], off
	v_lshl_add_u64 v[8:9], v[14:15], 0, s[54:55]
	s_mov_b32 m0, s69
	s_add_u32 s12, s34, 0x40080
	global_load_lds_dwordx4 v[8:9], off
	v_lshl_add_u64 v[8:9], v[16:17], 0, s[54:55]
	s_mov_b32 m0, s72
	s_addc_u32 s13, s35, 0
	s_add_i32 s73, s56, s7
	global_load_lds_dwordx4 v[8:9], off
	v_lshl_add_u64 v[8:9], s[12:13], 0, v[136:137]
	s_mov_b32 m0, s73
	s_add_i32 s86, s73, 0x2000
	global_load_lds_dwordx4 v[8:9], off
	v_lshl_add_u64 v[8:9], s[12:13], 0, v[132:133]
	s_mov_b32 m0, s86
	s_cmpk_lt_u32 s6, 0x100
	global_load_lds_dwordx4 v[8:9], off
	s_waitcnt vmcnt(8)
	s_barrier
	v_lshlrev_b32_e32 v8, 14, v6
	v_and_b32_e32 v8, 0xffff8000, v8
	v_lshl_add_u32 v5, v5, 11, v8
	v_and_b32_e32 v6, 1, v6
	v_lshl_or_b32 v5, v6, 6, v5
	v_lshl_add_u32 v140, v7, 1, v5
	v_lshlrev_b32_e32 v5, 14, v2
	v_and_b32_e32 v5, 0xffff8000, v5
	s_waitcnt vmcnt(6)
	v_lshl_add_u32 v3, v3, 11, v5
	v_and_b32_e32 v2, 1, v2
	v_lshl_or_b32 v2, v2, 6, v3
	s_cselect_b64 s[12:13], -1, 0
	v_or_b32_e32 v144, s18, v18
	v_mov_b32_e32 v141, v98
	v_lshl_add_u32 v142, v4, 1, v2
	v_mov_b32_e32 v143, v98
	s_mov_b32 s87, 0
	v_add_u32_e32 v145, s2, v19
	s_barrier
	s_branch .LBB13_1405

; #define PG8_STAGE_A(bufoff, h, ptr, nsel) do { if constexpr (Sched::GATHER) { if (nsel) PG8_STAGE_X(bufoff, ptr, vAn[h], PG8_A_AUX); else PG8_STAGE_X(bufoff, ptr, vAc[h], PG8_A_AUX); } \
;         else PG8_STAGE_X(bufoff, (ptr) + (h) * hstep, voffA, PG8_A_AUX); } while (0)
; #define PG8_STAGE(bufoff, gbase, voff) PG8_STAGE_X(bufoff, gbase, voff, PG8_B_AUX)
; #define PG8_WAIT_V(n) asm volatile("s_waitcnt vmcnt(" #n ")" ::: "memory")
; #define PG8_BAR __builtin_amdgcn_s_barrier()
; template <class Epi, class Sched, bool ALIGN_EPI = false, bool SP2 = false>
; __device__ __forceinline__ void gemm_phase(PG8_LAS unsigned char* lds, const Gemm g, const Sched& S, const Epi& E) {
;     ...
;         PG8_STAGE(PG8_SB(0, 0), cB, voffB); PG8_STAGE(PG8_SB(0, 1), cB + hstep, voffB); PG8_STAGE_A(PG8_SA(0, 0), 0, cA, false); PG8_STAGE_A(PG8_SA(0, 1), 1, cA, false);
;         if (wr == 1) PG8_BAR;
;         PG8_WAIT_V(2); PG8_BAR;
;         PG8_STAGE(PG8_SB(1, 0), cB + kstep, voffB); PG8_STAGE_A(PG8_SA(1, 0), 0, cA + kstep, false); PG8_STAGE(PG8_SB(1, 1), cB + hstep + kstep, voffB);
;         PG8_WAIT_V(6); PG8_BAR;
.LBB13_1430:
	v_lshrrev_b32_e32 v13, 1, v2
	v_and_b32_e32 v13, 24, v13
	v_and_b32_e32 v12, 15, v2
	v_lshlrev_b32_e32 v14, 1, v13
	v_lshlrev_b32_e32 v2, 2, v2
	v_lshl_or_b32 v244, s4, 6, v12
	v_lshl_or_b32 v12, v12, 6, v14
	s_lshl_b32 s4, s4, 13
	v_and_b32_e32 v2, 32, v2
	v_bitop3_b32 v14, v12, s4, v2 bitop3:0xde
	s_lshl_b32 s4, s6, 5
	s_and_b32 s22, s4, 0x60
	s_lshl_b32 s4, s22, 7
	s_add_u32 s6, s10, 0x20700080
	s_addc_u32 s7, s11, 0
	s_add_i32 s90, s51, s5
	v_lshl_add_u64 v[6:7], v[6:7], 0, s[54:55]
	s_mov_b32 m0, s90
	s_add_i32 s95, s90, 0x2000
	v_mov_b32_e32 v213, v98
	global_load_lds_dwordx4 v[6:7], off
	v_lshl_add_u64 v[6:7], v[8:9], 0, s[54:55]
	s_mov_b32 m0, s95
	s_add_i32 s64, s69, 0x8000
	v_mov_b32_e32 v10, v3
	v_mov_b32_e32 v11, v98
	s_add_i32 s94, s2, 0x20000
	global_load_lds_dwordx4 v[6:7], off
	v_lshl_add_u64 v[6:7], s[6:7], 0, v[212:213]
	s_mov_b32 m0, s64
	s_add_i32 s52, s69, 0xa000
	global_load_lds_dwordx4 v[6:7], off
	v_lshl_add_u64 v[6:7], s[6:7], 0, v[10:11]
	s_add_u32 s6, s34, 0x40080
	v_bitop3_b32 v245, v12, s4, v2 bitop3:0xde
	s_mov_b32 m0, s52
	s_addc_u32 s7, s35, 0
	s_add_i32 s4, s56, s5
	global_load_lds_dwordx4 v[6:7], off
	v_lshl_add_u64 v[6:7], s[6:7], 0, v[208:209]
	s_mov_b32 m0, s4
	s_add_i32 s5, s4, 0x2000
	global_load_lds_dwordx4 v[6:7], off
	v_lshl_add_u64 v[6:7], s[6:7], 0, v[210:211]
	s_mov_b32 m0, s5
	s_cmpk_lt_u32 s1, 0x100
	global_load_lds_dwordx4 v[6:7], off
	s_waitcnt vmcnt(8)
	s_barrier
	s_cselect_b64 s[20:21], -1, 0
	s_ashr_i32 s1, s0, 31
	s_lshr_b32 s6, s1, 29
	s_add_i32 s6, s0, s6
	s_ashr_i32 s86, s6, 3
	s_and_b32 s6, s6, -8
	s_waitcnt vmcnt(6)
	s_sub_i32 s87, s0, s6
	s_add_i32 s60, s86, 1
	v_readlane_b32 s6, v249, 33
	v_or_b32_e32 v246, s22, v13
	s_add_u32 s22, s6, s8
	v_readlane_b32 s6, v249, 34
	s_addc_u32 s23, s6, s9
	s_mov_b32 s72, 0
	v_add_u32_e32 v247, s2, v14
	s_barrier
	s_branch .LBB13_1433

; #define PG8_STAGE_A(bufoff, h, ptr, nsel) do { if constexpr (Sched::GATHER) { if (nsel) PG8_STAGE_X(bufoff, ptr, vAn[h], PG8_A_AUX); else PG8_STAGE_X(bufoff, ptr, vAc[h], PG8_A_AUX); } \
;         else PG8_STAGE_X(bufoff, (ptr) + (h) * hstep, voffA, PG8_A_AUX); } while (0)
; #define PG8_STAGE(bufoff, gbase, voff) PG8_STAGE_X(bufoff, gbase, voff, PG8_B_AUX)
; #define PG8_WAIT_V(n) asm volatile("s_waitcnt vmcnt(" #n ")" ::: "memory")
; #define PG8_BAR __builtin_amdgcn_s_barrier()
; template <class Epi, class Sched, bool ALIGN_EPI = false, bool SP2 = false>
; __device__ __forceinline__ void gemm_phase(PG8_LAS unsigned char* lds, const Gemm g, const Sched& S, const Epi& E) {
;     ...
;         PG8_STAGE(PG8_SB(0, 0), cB, voffB); PG8_STAGE(PG8_SB(0, 1), cB + hstep, voffB); PG8_STAGE_A(PG8_SA(0, 0), 0, cA, false); PG8_STAGE_A(PG8_SA(0, 1), 1, cA, false);
;         if (wr == 1) PG8_BAR;
;         PG8_WAIT_V(2); PG8_BAR;
;         PG8_STAGE(PG8_SB(1, 0), cB + kstep, voffB); PG8_STAGE_A(PG8_SA(1, 0), 0, cA + kstep, false); PG8_STAGE(PG8_SB(1, 1), cB + hstep + kstep, voffB);
;         PG8_WAIT_V(6); PG8_BAR;
.LBB13_1524:
	v_lshrrev_b32_e32 v20, 1, v18
	s_add_u32 s46, s27, 0x205000
	v_and_b32_e32 v20, 24, v20
	s_addc_u32 s47, s34, 0
	v_and_b32_e32 v19, 15, v18
	v_lshlrev_b32_e32 v21, 1, v20
	v_lshlrev_b32_e32 v18, 2, v18
	s_lshl_b32 s4, s4, 5
	s_add_i32 s48, s31, 0x18000
	v_lshl_or_b32 v166, s7, 6, v19
	v_lshl_or_b32 v19, v19, 6, v21
	s_lshl_b32 s7, s7, 13
	v_and_b32_e32 v18, 32, v18
	s_and_b32 s4, s4, 0x60
	s_add_i32 s49, s48, s5
	v_bitop3_b32 v21, v19, s7, v18 bitop3:0xde
	s_lshl_b32 s7, s4, 7
	v_lshl_add_u64 v[8:9], v[8:9], 0, s[54:55]
	s_mov_b32 m0, s49
	s_add_i32 s50, s49, 0x2000
	s_add_i32 s51, s42, 0x8000
	s_add_i32 s53, s42, 0xa000
	global_load_lds_dwordx4 v[8:9], off
	v_lshl_add_u64 v[6:7], v[6:7], 0, s[54:55]
	s_mov_b32 m0, s50
	s_add_u32 s12, s18, 0xb0080
	global_load_lds_dwordx4 v[6:7], off
	v_lshl_add_u64 v[2:3], v[2:3], 0, s[54:55]
	s_mov_b32 m0, s51
	s_addc_u32 s13, s19, 0
	s_add_i32 s56, s31, 0x1c000
	global_load_lds_dwordx4 v[2:3], off
	v_lshl_add_u64 v[2:3], v[4:5], 0, s[54:55]
	s_mov_b32 m0, s53
	s_add_i32 s57, s56, s5
	global_load_lds_dwordx4 v[2:3], off
	v_lshl_add_u64 v[2:3], s[12:13], 0, v[150:151]
	s_mov_b32 m0, s57
	s_add_i32 s58, s57, 0x2000
	global_load_lds_dwordx4 v[2:3], off
	v_lshl_add_u64 v[2:3], s[12:13], 0, v[154:155]
	s_mov_b32 m0, s58
	s_cmpk_lt_u32 s6, 0x100
	global_load_lds_dwordx4 v[2:3], off
	s_waitcnt vmcnt(8)
	s_barrier
	s_movk_i32 s6, 0xb00
	v_bitop3_b32 v167, v19, s7, v18 bitop3:0xde
	v_lshrrev_b32_e32 v3, 1, v10
	v_mul_lo_u32 v2, v12, s6
	s_mov_b32 s7, 0xb000
	v_or_b32_e32 v168, s4, v20
	v_mad_u64_u32 v[2:3], s[4:5], v3, s7, v[2:3]
	v_or_b32_e32 v2, v2, v11
	v_add_lshl_u32 v2, v2, v13, 1
	v_mov_b32_e32 v3, v98
	s_mov_b64 s[14:15], 0xb0080
	v_lshl_add_u64 v[156:157], v[2:3], 0, s[14:15]
	v_lshrrev_b32_e32 v3, 1, v14
	v_mul_lo_u32 v2, v16, s6
	v_mad_u64_u32 v[2:3], s[4:5], v3, s7, v[2:3]
	s_waitcnt vmcnt(6)
	v_or_b32_e32 v2, v2, v15
	v_add_lshl_u32 v2, v2, v17, 1
	v_mov_b32_e32 v3, v98
	s_cselect_b64 s[12:13], -1, 0
	s_ashr_i32 s59, s28, 31
	v_lshl_add_u64 v[158:159], v[2:3], 0, s[14:15]
	s_mov_b32 s61, 0
	v_add_u32_e32 v169, s31, v21
	s_barrier
	s_branch .LBB13_1527

; #define PG8_STAGE_A(bufoff, h, ptr, nsel) do { if constexpr (Sched::GATHER) { if (nsel) PG8_STAGE_X(bufoff, ptr, vAn[h], PG8_A_AUX); else PG8_STAGE_X(bufoff, ptr, vAc[h], PG8_A_AUX); } \
;         else PG8_STAGE_X(bufoff, (ptr) + (h) * hstep, voffA, PG8_A_AUX); } while (0)
; #define PG8_STAGE(bufoff, gbase, voff) PG8_STAGE_X(bufoff, gbase, voff, PG8_B_AUX)
; #define PG8_WAIT_V(n) asm volatile("s_waitcnt vmcnt(" #n ")" ::: "memory")
; #define PG8_BAR __builtin_amdgcn_s_barrier()
; template <class Epi, class Sched, bool ALIGN_EPI = false, bool SP2 = false>
; __device__ __forceinline__ void gemm_phase(PG8_LAS unsigned char* lds, const Gemm g, const Sched& S, const Epi& E) {
;     ...
;         PG8_STAGE(PG8_SB(0, 0), cB, voffB); PG8_STAGE(PG8_SB(0, 1), cB + hstep, voffB); PG8_STAGE_A(PG8_SA(0, 0), 0, cA, false); PG8_STAGE_A(PG8_SA(0, 1), 1, cA, false);
;         if (wr == 1) PG8_BAR;
;         PG8_WAIT_V(2); PG8_BAR;
;         PG8_STAGE(PG8_SB(1, 0), cB + kstep, voffB); PG8_STAGE_A(PG8_SA(1, 0), 0, cA + kstep, false); PG8_STAGE(PG8_SB(1, 1), cB + hstep + kstep, voffB);
;         PG8_WAIT_V(6); PG8_BAR;
.LBB13_1559:
	v_lshrrev_b32_e32 v20, 1, v10
	v_and_b32_e32 v20, 24, v20
	v_and_b32_e32 v19, 15, v10
	v_lshlrev_b32_e32 v21, 1, v20
	v_lshlrev_b32_e32 v10, 2, v10
	s_lshl_b32 s5, s5, 5
	s_add_i32 s58, s31, 0x18000
	v_lshl_or_b32 v144, s6, 6, v19
	v_lshl_or_b32 v19, v19, 6, v21
	s_lshl_b32 s6, s6, 13
	v_and_b32_e32 v10, 32, v10
	s_and_b32 s5, s5, 0x60
	s_add_i32 s59, s58, s4
	v_bitop3_b32 v21, v19, s6, v10 bitop3:0xde
	s_lshl_b32 s6, s5, 7
	v_lshl_add_u64 v[8:9], v[8:9], 0, s[54:55]
	s_mov_b32 m0, s59
	s_add_i32 s61, s59, 0x2000
	s_add_i32 s64, s52, 0x8000
	s_add_i32 s68, s52, 0xa000
	v_bitop3_b32 v145, v19, s6, v10 bitop3:0xde
	global_load_lds_dwordx4 v[8:9], off
	v_lshl_add_u64 v[6:7], v[6:7], 0, s[54:55]
	s_mov_b32 m0, s61
	s_add_u32 s6, s22, 0xe0080
	global_load_lds_dwordx4 v[6:7], off
	v_lshl_add_u64 v[2:3], v[2:3], 0, s[54:55]
	s_mov_b32 m0, s64
	s_addc_u32 s7, s23, 0
	s_add_i32 s69, s31, 0x1c000
	global_load_lds_dwordx4 v[2:3], off
	v_lshl_add_u64 v[2:3], v[4:5], 0, s[54:55]
	s_mov_b32 m0, s68
	s_add_i32 s72, s69, s4
	global_load_lds_dwordx4 v[2:3], off
	v_lshl_add_u64 v[2:3], s[6:7], 0, v[134:135]
	s_mov_b32 m0, s72
	s_add_i32 s73, s72, 0x2000
	global_load_lds_dwordx4 v[2:3], off
	v_lshl_add_u64 v[2:3], s[6:7], 0, v[138:139]
	s_mov_b32 m0, s73
	s_movk_i32 s7, 0xe00
	global_load_lds_dwordx4 v[2:3], off
	s_waitcnt vmcnt(8)
	s_barrier
	v_lshrrev_b32_e32 v3, 1, v12
	v_mul_lo_u32 v2, v15, s7
	s_mov_b32 s6, 0xe000
	v_or_b32_e32 v146, s5, v20
	v_mad_u64_u32 v[2:3], s[4:5], v3, s6, v[2:3]
	v_or_b32_e32 v2, v2, v14
	v_add_lshl_u32 v2, v2, v17, 1
	v_mov_b32_e32 v3, v98
	s_mov_b64 s[16:17], 0xe0080
	v_lshl_add_u64 v[140:141], v[2:3], 0, s[16:17]
	v_lshrrev_b32_e32 v3, 1, v11
	v_mul_lo_u32 v2, v16, s7
	v_mad_u64_u32 v[2:3], s[4:5], v3, s6, v[2:3]
	s_waitcnt vmcnt(6)
	v_or_b32_e32 v2, v2, v13
	s_cmpk_lt_u32 s14, 0x100
	v_add_lshl_u32 v2, v2, v18, 1
	v_mov_b32_e32 v3, v98
	s_cselect_b64 s[14:15], -1, 0
	v_lshl_add_u64 v[142:143], v[2:3], 0, s[16:17]
	s_mov_b32 s76, 0
	v_add_u32_e32 v147, s31, v21
	s_barrier
	s_branch .LBB13_1562
